# pssink1
# speedup vs baseline: 1.0061x; 1.0019x over previous
.LBB3_33:
	ds_read_b128 v[2:5], v217 offset:50176
	ds_read_b128 v[6:9], v217 offset:50304
	v_exp_f32_e32 v142, v142
	v_exp_f32_e32 v143, v143
	v_exp_f32_e32 v140, v140
	s_waitcnt vmcnt(1) lgkmcnt(1)
	v_mfma_f32_32x32x16_bf16 v[100:115], v[2:5], v[172:175], 0
	ds_read_b128 v[2:5], v217 offset:58880
	ds_read_b128 v[10:13], v217 offset:59008
	v_exp_f32_e32 v141, v141
	v_exp_f32_e32 v138, v138
	v_exp_f32_e32 v134, v134
	v_exp_f32_e32 v135, v135
	v_exp_f32_e32 v132, v132
	v_exp_f32_e32 v133, v133
	s_waitcnt lgkmcnt(1)
	v_mfma_f32_32x32x16_bf16 v[84:99], v[2:5], v[172:175], 0
	ds_read_b128 v[2:5], v217 offset:50208
	ds_read_b128 v[80:83], v217 offset:58912
	s_waitcnt vmcnt(0)
	ds_read_b128 v[116:119], v217 offset:50336
	v_exp_f32_e32 v130, v130
	v_exp_f32_e32 v131, v131
	v_exp_f32_e32 v128, v128
	v_exp_f32_e32 v129, v129
	s_sub_i32 s6, s60, 63
	s_waitcnt lgkmcnt(2)
	v_mfma_f32_32x32x16_bf16 v[100:115], v[2:5], v[168:171], v[100:115]
	ds_read_b128 v[2:5], v217 offset:59040
	ds_read_b128 v[120:123], v217 offset:50240
	ds_read_b128 v[124:127], v217 offset:50368
	ds_read_b128 v[230:233], v217 offset:58944
	ds_read_b128 v[234:237], v217 offset:59072
	ds_read_b128 v[238:241], v217 offset:50272
	ds_read_b128 v[242:245], v217 offset:50400
	s_waitcnt lgkmcnt(8)
	v_mfma_f32_32x32x16_bf16 v[84:99], v[80:83], v[168:171], v[84:99]
	ds_read_b128 v[80:83], v217 offset:58976
	ds_read_b128 v[246:249], v217 offset:59104
	s_waitcnt lgkmcnt(7)
	v_mfma_f32_32x32x16_bf16 v[100:115], v[120:123], v[164:167], v[100:115]
	v_add_f32_e32 v120, 0, v191
	v_add_f32_e32 v120, v193, v120
	v_add_f32_e32 v120, v189, v120
	v_add_f32_e32 v120, v192, v120
	v_add_f32_e32 v120, v188, v120
	v_add_f32_e32 v120, v190, v120
	v_add_f32_e32 v120, v186, v120
	s_waitcnt lgkmcnt(5)
	v_mfma_f32_32x32x16_bf16 v[84:99], v[230:233], v[164:167], v[84:99]
	v_add_f32_e32 v120, v187, v120
	v_add_f32_e32 v120, v179, v120
	v_add_f32_e32 v120, v184, v120
	v_exp_f32_e32 v122, v139
	v_exp_f32_e32 v123, v136
	v_exp_f32_e32 v136, v137
	s_waitcnt lgkmcnt(3)
	v_mfma_f32_32x32x16_bf16 v[100:115], v[238:241], v[148:151], v[100:115]
	s_waitcnt lgkmcnt(1)
	v_mfma_f32_32x32x16_bf16 v[84:99], v[80:83], v[148:151], v[84:99]
	v_add_f32_e32 v80, v177, v120
	v_add_f32_e32 v80, v182, v80
	v_add_f32_e32 v80, v176, v80
	v_add_f32_e32 v80, v185, v80
	v_add_f32_e32 v80, v178, v80
	v_add_f32_e32 v80, v183, v80
	v_add_f32_e32 v80, v142, v80
	v_mfma_f32_32x32x16_bf16 v[100:115], v[6:9], v[152:155], v[100:115]
	v_add_f32_e32 v6, v143, v80
	v_add_f32_e32 v6, v140, v6
	v_add_f32_e32 v6, v141, v6
	v_add_f32_e32 v6, v138, v6
	v_add_f32_e32 v6, v122, v6
	v_add_f32_e32 v6, v123, v6
	v_add_f32_e32 v6, v136, v6
	v_mfma_f32_32x32x16_bf16 v[84:99], v[10:13], v[152:155], v[84:99]
	v_add_f32_e32 v6, v134, v6
	v_add_f32_e32 v6, v135, v6
	v_add_f32_e32 v6, v132, v6
	v_add_f32_e32 v6, v133, v6
	v_add_f32_e32 v6, v130, v6
	v_add_f32_e32 v6, v131, v6
	v_add_f32_e32 v6, v128, v6
	v_mfma_f32_32x32x16_bf16 v[100:115], v[116:119], v[156:159], v[100:115]
	v_add_f32_e32 v199, v129, v6
	v_mov_b32_e32 v207, v199
	s_nop 1
	v_permlane32_swap_b32_e32 v199, v207
	v_cvt_pk_bf16_f32 v80, v191, v193
	v_cvt_pk_bf16_f32 v81, v189, v192
	v_cvt_pk_bf16_f32 v82, v188, v190
	v_mfma_f32_32x32x16_bf16 v[84:99], v[2:5], v[156:159], v[84:99]
	v_cvt_pk_bf16_f32 v83, v186, v187
	v_cvt_pk_bf16_f32 v116, v179, v184
	v_cvt_pk_bf16_f32 v117, v177, v182
	v_cvt_pk_bf16_f32 v118, v176, v185
	v_cvt_pk_bf16_f32 v119, v178, v183
	v_cvt_pk_bf16_f32 v120, v142, v143
	v_cvt_pk_bf16_f32 v121, v140, v141
	v_mfma_f32_32x32x16_bf16 v[100:115], v[124:127], v[160:163], v[100:115]
	v_cvt_pk_bf16_f32 v122, v138, v122
	v_cvt_pk_bf16_f32 v123, v123, v136
	v_cvt_pk_bf16_f32 v124, v134, v135
	v_cvt_pk_bf16_f32 v125, v132, v133
	v_cvt_pk_bf16_f32 v126, v130, v131
	v_cvt_pk_bf16_f32 v127, v128, v129
	v_permlane32_swap_b32_e32 v80, v82
	v_mfma_f32_32x32x16_bf16 v[84:99], v[234:237], v[160:163], v[84:99]
	v_permlane32_swap_b32_e32 v81, v83
	v_permlane32_swap_b32_e32 v116, v118
	v_permlane32_swap_b32_e32 v117, v119
	v_permlane32_swap_b32_e32 v120, v122
	v_mfma_f32_32x32x16_bf16 v[100:115], v[242:245], v[144:147], v[100:115]
	v_permlane32_swap_b32_e32 v121, v123
	v_permlane32_swap_b32_e32 v124, v126
	v_permlane32_swap_b32_e32 v125, v127
	s_waitcnt lgkmcnt(0)
	v_mfma_f32_32x32x16_bf16 v[84:99], v[246:249], v[144:147], v[84:99]
	v_add_u32_e32 v234, s60, v201
	v_add_u32_e32 v2, 1, v234
	v_add_u32_e32 v4, 33, v234
	v_ashrrev_i32_e32 v3, 31, v2
	v_ashrrev_i32_e32 v5, 31, v4
	v_lshlrev_b64 v[10:11], 8, v[2:3]
	v_lshlrev_b64 v[12:13], 8, v[4:5]
	v_lshl_add_u64 v[2:3], v[14:15], 0, v[10:11]
	v_lshl_add_u64 v[6:7], v[14:15], 0, v[12:13]
	v_lshl_add_u64 v[10:11], v[208:209], 0, v[10:11]
	global_load_dwordx4 v[2:5], v[2:3], off
	s_nop 0
	global_load_dwordx4 v[6:9], v[6:7], off
	v_lshl_add_u64 v[128:129], v[208:209], 0, v[12:13]
	global_load_dwordx4 v[10:13], v[10:11], off
	s_nop 0
	global_load_dwordx4 v[176:179], v[128:129], off
	ds_read_b64_tr_b16 v[128:129], v213 offset:0
	ds_read_b64_tr_b16 v[130:131], v213 offset:0x800
	ds_read_b64_tr_b16 v[132:133], v213 offset:0x1000
	ds_read_b64_tr_b16 v[134:135], v213 offset:0x1800
	ds_read_b64_tr_b16 v[136:137], v213 offset:0x2000
	ds_read_b64_tr_b16 v[138:139], v213 offset:0x2800
	ds_read_b64_tr_b16 v[140:141], v213 offset:0x3000
	ds_read_b64_tr_b16 v[142:143], v213 offset:0x3800
	s_nop 0
	s_waitcnt lgkmcnt(6)
	v_mfma_f32_32x32x16_bf16 v[64:79], v[80:83], v[128:131], v[64:79]
	ds_read_b64_tr_b16 v[128:129], v213 offset:0x200
	ds_read_b64_tr_b16 v[130:131], v213 offset:0xa00
	s_waitcnt lgkmcnt(6)
	v_mfma_f32_32x32x16_bf16 v[64:79], v[116:119], v[132:135], v[64:79]
	ds_read_b64_tr_b16 v[132:133], v213 offset:0x1200
	ds_read_b64_tr_b16 v[134:135], v213 offset:0x1a00
	s_waitcnt lgkmcnt(6)
	v_mfma_f32_32x32x16_bf16 v[64:79], v[120:123], v[136:139], v[64:79]
	ds_read_b64_tr_b16 v[136:137], v213 offset:0x2200
	ds_read_b64_tr_b16 v[138:139], v213 offset:0x2a00
	ds_read_b64_tr_b16 v[182:183], v213 offset:0x3200
	ds_read_b64_tr_b16 v[184:185], v213 offset:0x3a00
	s_waitcnt lgkmcnt(8)
	v_mfma_f32_32x32x16_bf16 v[64:79], v[124:127], v[140:143], v[64:79]
	s_waitcnt lgkmcnt(6)
	v_mfma_f32_32x32x16_bf16 v[48:63], v[80:83], v[128:131], v[48:63]
	ds_read_b64_tr_b16 v[128:129], v213 offset:0x400
	ds_read_b64_tr_b16 v[130:131], v213 offset:0xc00
	s_waitcnt lgkmcnt(6)
	v_mfma_f32_32x32x16_bf16 v[48:63], v[116:119], v[132:135], v[48:63]
	ds_read_b64_tr_b16 v[132:133], v213 offset:0x1400
	ds_read_b64_tr_b16 v[134:135], v213 offset:0x1c00
	s_waitcnt lgkmcnt(6)
	v_mfma_f32_32x32x16_bf16 v[48:63], v[120:123], v[136:139], v[48:63]
	ds_read_b64_tr_b16 v[136:137], v213 offset:0x2400
	ds_read_b64_tr_b16 v[138:139], v213 offset:0x2c00
	ds_read_b64_tr_b16 v[140:141], v213 offset:0x3400
	ds_read_b64_tr_b16 v[142:143], v213 offset:0x3c00
	s_waitcnt lgkmcnt(8)
	v_mfma_f32_32x32x16_bf16 v[48:63], v[124:127], v[182:185], v[48:63]
	s_cmp_le_i32 s60, s55
	s_cselect_b64 s[46:47], -1, 0
	s_cmp_gt_i32 s6, s56
	s_cselect_b64 s[6:7], -1, 0
	s_and_b64 s[6:7], s[46:47], s[6:7]
	s_and_b64 vcc, exec, s[6:7]
	s_cbranch_vccnz .LBB3_35
	v_add_u32_e32 v219, 123, v0
	v_cmp_ge_i32_e64 s[64:65], v219, 0
	v_cmp_ge_i32_e64 s[66:67], v219, 32
	v_cmp_ge_i32_e64 s[68:69], v219, 1
	v_cmp_ge_i32_e64 s[70:71], v219, 33
	v_cmp_ge_i32_e64 s[72:73], v219, 2
	v_cmp_ge_i32_e64 s[74:75], v219, 34
	v_cmp_ge_i32_e64 s[76:77], v219, 3
	v_cmp_ge_i32_e64 s[78:79], v219, 35
	v_cndmask_b32_e64 v100, v221, v100, s[64:65]
	v_cndmask_b32_e64 v84, v221, v84, s[66:67]
	v_cndmask_b32_e64 v101, v221, v101, s[68:69]
	v_cndmask_b32_e64 v85, v221, v85, s[70:71]
	v_cndmask_b32_e64 v102, v221, v102, s[72:73]
	v_cndmask_b32_e64 v86, v221, v86, s[74:75]
	v_cndmask_b32_e64 v103, v221, v103, s[76:77]
	v_cndmask_b32_e64 v87, v221, v87, s[78:79]
	v_cmp_ge_i32_e64 s[64:65], v219, 8
	v_cmp_ge_i32_e64 s[66:67], v219, 40
	v_cmp_ge_i32_e64 s[68:69], v219, 9
	v_cmp_ge_i32_e64 s[70:71], v219, 41
	v_cmp_ge_i32_e64 s[72:73], v219, 10
	v_cmp_ge_i32_e64 s[74:75], v219, 42
	v_cmp_ge_i32_e64 s[76:77], v219, 11
	v_cmp_ge_i32_e64 s[78:79], v219, 43
	v_cndmask_b32_e64 v104, v221, v104, s[64:65]
	v_cndmask_b32_e64 v88, v221, v88, s[66:67]
	v_cndmask_b32_e64 v105, v221, v105, s[68:69]
	v_cndmask_b32_e64 v89, v221, v89, s[70:71]
	v_cndmask_b32_e64 v106, v221, v106, s[72:73]
	v_cndmask_b32_e64 v90, v221, v90, s[74:75]
	v_cndmask_b32_e64 v107, v221, v107, s[76:77]
	v_cndmask_b32_e64 v91, v221, v91, s[78:79]
	v_cmp_ge_i32_e64 s[64:65], v219, 16
	v_cmp_ge_i32_e64 s[66:67], v219, 48
	v_cmp_ge_i32_e64 s[68:69], v219, 17
	v_cmp_ge_i32_e64 s[70:71], v219, 49
	v_cmp_ge_i32_e64 s[72:73], v219, 18
	v_cmp_ge_i32_e64 s[74:75], v219, 50
	v_cmp_ge_i32_e64 s[76:77], v219, 19
	v_cmp_ge_i32_e64 s[78:79], v219, 51
	v_cndmask_b32_e64 v108, v221, v108, s[64:65]
	v_cndmask_b32_e64 v92, v221, v92, s[66:67]
	v_cndmask_b32_e64 v109, v221, v109, s[68:69]
	v_cndmask_b32_e64 v93, v221, v93, s[70:71]
	v_cndmask_b32_e64 v110, v221, v110, s[72:73]
	v_cndmask_b32_e64 v94, v221, v94, s[74:75]
	v_cndmask_b32_e64 v111, v221, v111, s[76:77]
	v_cndmask_b32_e64 v95, v221, v95, s[78:79]
	v_cmp_ge_i32_e64 s[64:65], v219, 24
	v_cmp_ge_i32_e64 s[66:67], v219, 56
	v_cmp_ge_i32_e64 s[68:69], v219, 25
	v_cmp_ge_i32_e64 s[70:71], v219, 57
	v_cmp_ge_i32_e64 s[72:73], v219, 26
	v_cmp_ge_i32_e64 s[74:75], v219, 58
	v_cmp_ge_i32_e64 s[76:77], v219, 27
	v_cmp_ge_i32_e64 s[78:79], v219, 59
	v_cndmask_b32_e64 v112, v221, v112, s[64:65]
	v_cndmask_b32_e64 v96, v221, v96, s[66:67]
	v_cndmask_b32_e64 v113, v221, v113, s[68:69]
	v_cndmask_b32_e64 v97, v221, v97, s[70:71]
	v_cndmask_b32_e64 v114, v221, v114, s[72:73]
	v_cndmask_b32_e64 v98, v221, v98, s[74:75]
	v_cndmask_b32_e64 v115, v221, v115, s[76:77]
	v_cndmask_b32_e64 v99, v221, v99, s[78:79]
.LBB3_35:
	s_waitcnt lgkmcnt(6)
	v_mfma_f32_32x32x16_bf16 v[32:47], v[80:83], v[128:131], v[32:47]
	v_max_f32_e32 v218, v101, v101
	v_max_f32_e32 v219, v100, v100
	v_max_f32_e32 v218, v219, v218
	v_max3_f32 v218, v218, v102, v103
	v_max3_f32 v218, v218, v104, v105
	ds_read_b64_tr_b16 v[128:129], v213 offset:0x600
	ds_read_b64_tr_b16 v[130:131], v213 offset:0xe00
	s_waitcnt lgkmcnt(6)
	v_mfma_f32_32x32x16_bf16 v[32:47], v[116:119], v[132:135], v[32:47]
	v_max3_f32 v218, v218, v106, v107
	v_max3_f32 v218, v218, v108, v109
	v_max3_f32 v218, v218, v110, v111
	v_max3_f32 v218, v218, v112, v113
	v_max3_f32 v218, v218, v114, v115
	ds_read_b64_tr_b16 v[132:133], v213 offset:0x1600
	ds_read_b64_tr_b16 v[134:135], v213 offset:0x1e00
	s_waitcnt lgkmcnt(6)
	v_mfma_f32_32x32x16_bf16 v[32:47], v[120:123], v[136:139], v[32:47]
	v_max3_f32 v218, v218, v84, v85
	v_max3_f32 v218, v218, v86, v87
	v_max3_f32 v218, v218, v88, v89
	v_max3_f32 v218, v218, v90, v91
	v_max3_f32 v218, v218, v92, v93
	ds_read_b64_tr_b16 v[136:137], v213 offset:0x2600
	ds_read_b64_tr_b16 v[138:139], v213 offset:0x2e00
	ds_read_b64_tr_b16 v[182:183], v213 offset:0x3600
	ds_read_b64_tr_b16 v[184:185], v213 offset:0x3e00
	s_waitcnt lgkmcnt(8)
	v_mfma_f32_32x32x16_bf16 v[32:47], v[124:127], v[140:143], v[32:47]
	v_max3_f32 v218, v218, v94, v95
	v_max3_f32 v218, v218, v96, v97
	v_max3_f32 v218, v218, v98, v99
	v_mov_b32_e32 v219, v218
	s_nop 1
	v_permlane32_swap_b32_e32 v218, v219
	s_waitcnt lgkmcnt(6)
	v_mfma_f32_32x32x16_bf16 v[16:31], v[80:83], v[128:131], v[16:31]
	v_max_f32_e32 v219, v219, v219
	v_max_f32_e32 v218, v218, v218
	v_max_f32_e32 v218, v218, v219
	v_max_f32_e32 v220, v180, v180
	v_sub_f32_e32 v219, v218, v180
	s_waitcnt lgkmcnt(4)
	v_mfma_f32_32x32x16_bf16 v[16:31], v[116:119], v[132:135], v[16:31]
	v_max_f32_e32 v218, v220, v218
	v_sub_f32_e32 v220, v180, v218
	v_mul_f32_e32 v220, 0x3e0293ee, v220
	v_mul_f32_e32 v219, 0x3db504f3, v219
	v_exp_f32_e32 v220, v220
	s_waitcnt lgkmcnt(2)
	v_mfma_f32_32x32x16_bf16 v[16:31], v[120:123], v[136:139], v[16:31]
	s_waitcnt lgkmcnt(0)
	v_mfma_f32_32x32x16_bf16 v[16:31], v[124:127], v[182:185], v[16:31]
	v_cmp_ge_f32_e32 vcc, s20, v219
	s_cmp_eq_u64 vcc, exec
	s_cselect_b64 s[6:7], -1, 0
	s_barrier
	s_waitcnt vmcnt(0)
	v_cndmask_b32_e64 v230, v220, 1.0, s[6:7]
	v_cmp_gt_f32_e32 vcc, 1.0, v230
	s_waitcnt vmcnt(3)
	ds_write_b128 v215, v[2:5]
	s_waitcnt vmcnt(2)
	ds_write_b128 v216, v[6:9]
	s_waitcnt vmcnt(1)
	ds_write_b128 v222, v[10:13] offset:32768
	s_waitcnt vmcnt(0)
	ds_write_b128 v222, v[176:179] offset:41472
	s_cbranch_vccz .LBB3_39
	s_and_saveexec_b64 s[46:47], s[0:1]
	ds_write_b32 v226, v230 offset:128
	s_or_b64 exec, exec, s[46:47]
	s_waitcnt lgkmcnt(0)
	ds_read_b128 v[116:119], v225 offset:224
	ds_read_b128 v[120:123], v225 offset:192
	ds_read_b128 v[124:127], v225 offset:160
	ds_read_b128 v[128:131], v225 offset:128
	s_waitcnt lgkmcnt(3)
	v_pk_mul_f32 v[78:79], v[78:79], v[118:119]
	s_waitcnt lgkmcnt(2)
	v_pk_mul_f32 v[74:75], v[74:75], v[122:123]
	s_waitcnt lgkmcnt(1)
	v_pk_mul_f32 v[70:71], v[70:71], v[126:127]
	s_waitcnt lgkmcnt(0)
	v_pk_mul_f32 v[66:67], v[66:67], v[130:131]
	v_pk_mul_f32 v[76:77], v[76:77], v[116:117]
	v_pk_mul_f32 v[72:73], v[72:73], v[120:121]
	v_pk_mul_f32 v[68:69], v[68:69], v[124:125]
	v_pk_mul_f32 v[64:65], v[64:65], v[128:129]
	v_pk_mul_f32 v[62:63], v[62:63], v[118:119]
	v_pk_mul_f32 v[58:59], v[58:59], v[122:123]
	v_pk_mul_f32 v[54:55], v[54:55], v[126:127]
	v_pk_mul_f32 v[50:51], v[50:51], v[130:131]
	v_pk_mul_f32 v[60:61], v[60:61], v[116:117]
	v_pk_mul_f32 v[56:57], v[56:57], v[120:121]
	v_pk_mul_f32 v[52:53], v[52:53], v[124:125]
	v_pk_mul_f32 v[48:49], v[48:49], v[128:129]
	v_pk_mul_f32 v[46:47], v[46:47], v[118:119]
	v_pk_mul_f32 v[42:43], v[42:43], v[122:123]
	v_pk_mul_f32 v[38:39], v[38:39], v[126:127]
	v_pk_mul_f32 v[34:35], v[34:35], v[130:131]
	v_pk_mul_f32 v[44:45], v[44:45], v[116:117]
	v_pk_mul_f32 v[40:41], v[40:41], v[120:121]
	v_pk_mul_f32 v[36:37], v[36:37], v[124:125]
	v_pk_mul_f32 v[32:33], v[32:33], v[128:129]
	v_pk_mul_f32 v[30:31], v[30:31], v[118:119]
	v_pk_mul_f32 v[26:27], v[26:27], v[122:123]
	v_pk_mul_f32 v[22:23], v[22:23], v[126:127]
	v_pk_mul_f32 v[18:19], v[18:19], v[130:131]
	v_pk_mul_f32 v[28:29], v[28:29], v[116:117]
	v_pk_mul_f32 v[24:25], v[24:25], v[120:121]
	v_pk_mul_f32 v[20:21], v[20:21], v[124:125]
	v_pk_mul_f32 v[16:17], v[16:17], v[128:129]
.LBB3_39:
	v_cndmask_b32_e64 v231, v218, v180, s[6:7]
	v_mul_f32_e32 v180, 0xbe0293ee, v231
	v_fmamk_f32 v80, v100, 0x3e0293ee, v180
	v_fmamk_f32 v81, v101, 0x3e0293ee, v180
	v_fmamk_f32 v82, v102, 0x3e0293ee, v180
	v_fmamk_f32 v83, v103, 0x3e0293ee, v180
	v_fmamk_f32 v116, v104, 0x3e0293ee, v180
	v_fmamk_f32 v117, v105, 0x3e0293ee, v180
	v_fmamk_f32 v118, v106, 0x3e0293ee, v180
	v_fmamk_f32 v119, v107, 0x3e0293ee, v180
	v_fmamk_f32 v120, v108, 0x3e0293ee, v180
	v_fmamk_f32 v121, v109, 0x3e0293ee, v180
	v_fmamk_f32 v122, v110, 0x3e0293ee, v180
	v_fmamk_f32 v123, v111, 0x3e0293ee, v180
	v_fmamk_f32 v112, v112, 0x3e0293ee, v180
	v_fmamk_f32 v113, v113, 0x3e0293ee, v180
	v_fmamk_f32 v114, v114, 0x3e0293ee, v180
	v_fmamk_f32 v115, v115, 0x3e0293ee, v180
	v_fmamk_f32 v100, v84, 0x3e0293ee, v180
	v_fmamk_f32 v109, v85, 0x3e0293ee, v180
	v_fmamk_f32 v110, v86, 0x3e0293ee, v180
	v_fmamk_f32 v111, v87, 0x3e0293ee, v180
	v_fmamk_f32 v181, v88, 0x3e0293ee, v180
	v_fmamk_f32 v101, v89, 0x3e0293ee, v180
	v_fmamk_f32 v102, v90, 0x3e0293ee, v180
	v_fmamk_f32 v103, v91, 0x3e0293ee, v180
	v_fmamk_f32 v104, v92, 0x3e0293ee, v180
	v_fmamk_f32 v105, v93, 0x3e0293ee, v180
	v_fmamk_f32 v106, v94, 0x3e0293ee, v180
	v_fmamk_f32 v107, v95, 0x3e0293ee, v180
	v_exp_f32_e32 v80, v80
	v_exp_f32_e32 v81, v81
	v_exp_f32_e32 v82, v82
	v_exp_f32_e32 v83, v83
	v_exp_f32_e32 v84, v116
	v_exp_f32_e32 v85, v117
	v_exp_f32_e32 v86, v118
	v_exp_f32_e32 v87, v119
	v_exp_f32_e32 v88, v120
	v_exp_f32_e32 v89, v121
	v_exp_f32_e32 v90, v122
	v_exp_f32_e32 v91, v123
	v_exp_f32_e32 v92, v112
	v_exp_f32_e32 v93, v113
	v_exp_f32_e32 v94, v114
	v_exp_f32_e32 v95, v115
	v_fmamk_f32 v108, v96, 0x3e0293ee, v180
	v_fmamk_f32 v182, v97, 0x3e0293ee, v180
	v_fmamk_f32 v183, v98, 0x3e0293ee, v180
	v_fmac_f32_e32 v180, 0x3e0293ee, v99
	s_waitcnt lgkmcnt(0)
	s_barrier
	ds_read_b128 v[96:99], v217 offset:32768
	ds_read_b128 v[112:115], v217 offset:41472
	ds_read_b128 v[2:5], v217 offset:32800
	ds_read_b128 v[6:9], v217 offset:41504
	ds_read_b128 v[10:13], v217 offset:32832
	ds_read_b128 v[176:179], v217 offset:41536
	v_exp_f32_e32 v101, v101
	v_exp_f32_e32 v102, v102
	v_exp_f32_e32 v103, v103
	s_waitcnt lgkmcnt(5)
	v_mfma_f32_32x32x16_bf16 v[128:143], v[96:99], v[172:175], 0
	v_exp_f32_e32 v104, v104
	v_exp_f32_e32 v105, v105
	v_exp_f32_e32 v106, v106
	v_exp_f32_e32 v107, v107
	v_exp_f32_e32 v108, v108
	s_waitcnt lgkmcnt(4)
	v_mfma_f32_32x32x16_bf16 v[112:127], v[112:115], v[172:175], 0
	ds_read_b128 v[96:99], v217 offset:32864
	ds_read_b128 v[184:187], v217 offset:41568
	s_waitcnt lgkmcnt(5)
	v_mfma_f32_32x32x16_bf16 v[128:143], v[2:5], v[168:171], v[128:143]
	s_waitcnt lgkmcnt(4)
	v_mfma_f32_32x32x16_bf16 v[112:127], v[6:9], v[168:171], v[112:127]
	ds_read_b128 v[2:5], v217 offset:32896
	ds_read_b128 v[6:9], v217 offset:41600
	s_waitcnt lgkmcnt(5)
	v_mfma_f32_32x32x16_bf16 v[128:143], v[10:13], v[164:167], v[128:143]
	s_waitcnt lgkmcnt(4)
	v_mfma_f32_32x32x16_bf16 v[112:127], v[176:179], v[164:167], v[112:127]
	ds_read_b128 v[10:13], v217 offset:32928
	ds_read_b128 v[176:179], v217 offset:41632
	s_waitcnt lgkmcnt(5)
	v_mfma_f32_32x32x16_bf16 v[128:143], v[96:99], v[148:151], v[128:143]
	s_waitcnt lgkmcnt(4)
	v_mfma_f32_32x32x16_bf16 v[112:127], v[184:187], v[148:151], v[112:127]
	ds_read_b128 v[96:99], v217 offset:32960
	ds_read_b128 v[184:187], v217 offset:41664
	s_waitcnt lgkmcnt(5)
	v_mfma_f32_32x32x16_bf16 v[128:143], v[2:5], v[152:155], v[128:143]
	s_waitcnt lgkmcnt(4)
	v_mfma_f32_32x32x16_bf16 v[112:127], v[6:9], v[152:155], v[112:127]
	ds_read_b128 v[2:5], v217 offset:32992
	ds_read_b128 v[6:9], v217 offset:41696
	s_waitcnt lgkmcnt(5)
	v_mfma_f32_32x32x16_bf16 v[128:143], v[10:13], v[156:159], v[128:143]
	s_waitcnt lgkmcnt(4)
	v_mfma_f32_32x32x16_bf16 v[112:127], v[176:179], v[156:159], v[112:127]
	s_waitcnt lgkmcnt(3)
	v_mfma_f32_32x32x16_bf16 v[128:143], v[96:99], v[160:163], v[128:143]
	s_waitcnt lgkmcnt(2)
	v_mfma_f32_32x32x16_bf16 v[112:127], v[184:187], v[160:163], v[112:127]
	s_waitcnt lgkmcnt(1)
	v_mfma_f32_32x32x16_bf16 v[128:143], v[2:5], v[144:147], v[128:143]
	v_exp_f32_e32 v99, v111
	v_exp_f32_e32 v111, v180
	v_add_f32_e32 v180, 0, v80
	v_add_f32_e32 v180, v81, v180
	v_add_f32_e32 v180, v82, v180
	v_add_f32_e32 v180, v83, v180
	v_add_f32_e32 v180, v84, v180
	v_add_f32_e32 v180, v85, v180
	v_add_f32_e32 v180, v86, v180
	v_add_f32_e32 v180, v87, v180
	v_add_f32_e32 v180, v88, v180
	v_add_f32_e32 v180, v89, v180
	v_add_f32_e32 v180, v90, v180
	v_add_f32_e32 v180, v91, v180
	v_exp_f32_e32 v96, v100
	v_add_f32_e32 v180, v92, v180
	v_exp_f32_e32 v97, v109
	v_add_f32_e32 v180, v93, v180
	v_exp_f32_e32 v98, v110
	v_add_f32_e32 v180, v94, v180
	v_add_f32_e32 v180, v95, v180
	v_exp_f32_e32 v100, v181
	v_add_f32_e32 v180, v96, v180
	v_add_f32_e32 v180, v97, v180
	v_add_f32_e32 v180, v98, v180
	v_add_f32_e32 v180, v99, v180
	v_add_f32_e32 v180, v100, v180
	v_add_f32_e32 v180, v101, v180
	v_add_f32_e32 v180, v102, v180
	v_add_f32_e32 v180, v103, v180
	v_add_f32_e32 v180, v104, v180
	v_exp_f32_e32 v109, v182
	v_add_f32_e32 v180, v105, v180
	s_waitcnt lgkmcnt(0)
	v_mfma_f32_32x32x16_bf16 v[112:127], v[6:9], v[144:147], v[112:127]
	v_exp_f32_e32 v110, v183
	v_add_f32_e32 v180, v106, v180
	v_add_f32_e32 v180, v107, v180
	v_add_f32_e32 v180, v108, v180
	v_add_f32_e32 v180, v109, v180
	v_add_f32_e32 v180, v110, v180
	v_add_f32_e32 v232, v111, v180
	v_mov_b32_e32 v233, v232
	v_cvt_pk_bf16_f32 v180, v80, v81
	v_cvt_pk_bf16_f32 v181, v82, v83
	v_cvt_pk_bf16_f32 v182, v84, v85
	v_cvt_pk_bf16_f32 v183, v86, v87
	v_cvt_pk_bf16_f32 v184, v88, v89
	v_cvt_pk_bf16_f32 v185, v90, v91
	v_cvt_pk_bf16_f32 v186, v92, v93
	v_cvt_pk_bf16_f32 v187, v94, v95
	v_cvt_pk_bf16_f32 v188, v96, v97
	v_cvt_pk_bf16_f32 v189, v98, v99
	v_cvt_pk_bf16_f32 v190, v100, v101
	v_cvt_pk_bf16_f32 v191, v102, v103
	v_cvt_pk_bf16_f32 v192, v104, v105
	v_cvt_pk_bf16_f32 v193, v106, v107
	v_cvt_pk_bf16_f32 v194, v108, v109
	v_cvt_pk_bf16_f32 v195, v110, v111
	s_nop 1
	v_permlane32_swap_b32_e32 v232, v233
	v_permlane32_swap_b32_e32 v180, v182
	v_permlane32_swap_b32_e32 v181, v183
	v_permlane32_swap_b32_e32 v184, v186
	v_permlane32_swap_b32_e32 v185, v187
	v_permlane32_swap_b32_e32 v188, v190
	v_permlane32_swap_b32_e32 v189, v191
	v_permlane32_swap_b32_e32 v192, v194
	v_permlane32_swap_b32_e32 v193, v195
	s_add_i32 s6, s59, 1
	s_cmp_lt_i32 s6, s58
	s_cselect_b64 s[46:47], -1, 0
	s_cmp_ge_i32 s6, s58
	s_cbranch_scc1 .LBB3_41
	v_add_u32_e32 v2, 0x41, v234
	v_add_u32_e32 v4, 0x61, v234
	v_ashrrev_i32_e32 v3, 31, v2
	v_ashrrev_i32_e32 v5, 31, v4
	v_lshlrev_b64 v[10:11], 8, v[2:3]
	v_lshlrev_b64 v[12:13], 8, v[4:5]
	v_lshl_add_u64 v[2:3], v[14:15], 0, v[10:11]
	v_lshl_add_u64 v[6:7], v[14:15], 0, v[12:13]
	v_lshl_add_u64 v[10:11], v[208:209], 0, v[10:11]
	v_lshl_add_u64 v[176:177], v[208:209], 0, v[12:13]
	global_load_dwordx4 v[2:5], v[2:3], off
	s_nop 0
	global_load_dwordx4 v[6:9], v[6:7], off
	s_nop 0
	global_load_dwordx4 v[10:13], v[10:11], off
	s_nop 0
	global_load_dwordx4 v[176:179], v[176:177], off
